# load_moe_table: the 16 expert-counter reads issued together instead of 16 serialized round trips (4 call sites)
# speedup vs baseline: 1.0161x; 1.0161x over previous
.LBB0_248:
	s_andn2_b64 vcc, exec, s[4:5]
	v_readlane_b32 s4, v255, 21
	v_readlane_b32 s5, v255, 22
	s_xor_b64 s[4:5], s[4:5], -1
	v_writelane_b32 v255, s4, 37
	s_nop 1
	v_writelane_b32 v255, s5, 38
	s_cbranch_vccnz .LBB0_330
	s_mov_b64 s[44:45], s[70:71]
	v_mbcnt_lo_u32_b32 v67, -1, 0
	v_mbcnt_hi_u32_b32 v67, -1, v67
	s_load_dwordx2 s[46:47], s[44:45], 0x100
	v_add_u32_e32 v0, s67, v67
	v_readlane_b32 s6, v255, 37
	v_readfirstlane_b32 s4, v0
	s_ashr_i32 s12, s4, 6
	s_waitcnt lgkmcnt(0)
	s_add_u32 s10, s46, 0x100000
	v_readlane_b32 s7, v255, 38
	v_and_b32_e32 v66, 63, v67
	s_addc_u32 s11, s47, 0
	s_mov_b64 s[4:5], -1
	s_and_b64 vcc, exec, s[6:7]
	s_cbranch_vccz .LBB0_269
	v_cmp_eq_u32_e32 vcc, 0, v0
	s_and_saveexec_b64 s[4:5], vcc
	s_cbranch_execz .LBB0_252
	v_mov_b32_e32 v6, 0x10000
	global_load_dword v0, v6, s[46:47] sc1
	v_readlane_b32 s6, v254, 50
	v_mov_b32_e32 v3, s81
	ds_write_b32 v3, v1
	v_mov_b32_e32 v2, s6
	v_readlane_b32 s6, v254, 51
	s_waitcnt vmcnt(0)
	v_min_i32_e32 v0, 0x4000, v0
	ds_write_b32 v2, v0
	global_load_dword v8, v6, s[46:47] offset:256 sc1
	global_load_dword v9, v6, s[46:47] offset:512 sc1
	global_load_dword v10, v6, s[46:47] offset:768 sc1
	global_load_dword v11, v6, s[46:47] offset:1024 sc1
	global_load_dword v12, v6, s[46:47] offset:1280 sc1
	global_load_dword v13, v6, s[46:47] offset:1536 sc1
	global_load_dword v14, v6, s[46:47] offset:1792 sc1
	global_load_dword v15, v6, s[46:47] offset:2048 sc1
	global_load_dword v16, v6, s[46:47] offset:2304 sc1
	global_load_dword v17, v6, s[46:47] offset:2560 sc1
	global_load_dword v18, v6, s[46:47] offset:2816 sc1
	global_load_dword v19, v6, s[46:47] offset:3072 sc1
	global_load_dword v20, v6, s[46:47] offset:3328 sc1
	global_load_dword v21, v6, s[46:47] offset:3584 sc1
	global_load_dword v22, v6, s[46:47] offset:3840 sc1
	v_mov_b32_e32 v3, s6
	v_readlane_b32 s6, v254, 52
	v_add_u32_e32 v0, 0xff, v0
	v_ashrrev_i32_e32 v0, 8, v0
	v_mov_b32_e32 v4, s6
	ds_write_b32 v4, v0
	v_readlane_b32 s6, v254, 53
	s_waitcnt vmcnt(0)
	v_min_i32_e32 v2, 0x4000, v8
	ds_write_b32 v3, v2
	v_add_u32_e32 v2, 0xff, v2
	v_mov_b32_e32 v4, s6
	v_readlane_b32 s6, v254, 54
	v_ashrrev_i32_e32 v2, 8, v2
	v_add_u32_e32 v0, v2, v0
	v_mov_b32_e32 v5, s6
	ds_write_b32 v5, v0
	v_readlane_b32 s6, v254, 55
	s_waitcnt vmcnt(0)
	v_min_i32_e32 v2, 0x4000, v9
	ds_write_b32 v4, v2
	v_add_u32_e32 v2, 0xff, v2
	v_mov_b32_e32 v4, s6
	v_readlane_b32 s6, v254, 56
	v_ashrrev_i32_e32 v2, 8, v2
	v_add_u32_e32 v0, v2, v0
	v_mov_b32_e32 v5, s6
	ds_write_b32 v5, v0
	v_readlane_b32 s6, v254, 57
	s_waitcnt vmcnt(0)
	v_min_i32_e32 v2, 0x4000, v10
	ds_write_b32 v4, v2
	v_add_u32_e32 v2, 0xff, v2
	v_mov_b32_e32 v4, s6
	v_readlane_b32 s6, v254, 58
	v_ashrrev_i32_e32 v2, 8, v2
	v_add_u32_e32 v0, v2, v0
	v_mov_b32_e32 v5, s6
	ds_write_b32 v5, v0
	v_readlane_b32 s6, v254, 59
	s_waitcnt vmcnt(0)
	v_min_i32_e32 v2, 0x4000, v11
	ds_write_b32 v4, v2
	v_add_u32_e32 v2, 0xff, v2
	v_mov_b32_e32 v4, s6
	v_readlane_b32 s6, v254, 60
	v_ashrrev_i32_e32 v2, 8, v2
	v_add_u32_e32 v0, v2, v0
	v_mov_b32_e32 v5, s6
	ds_write_b32 v5, v0
	v_readlane_b32 s6, v254, 61
	s_waitcnt vmcnt(0)
	v_min_i32_e32 v2, 0x4000, v12
	ds_write_b32 v4, v2
	v_add_u32_e32 v2, 0xff, v2
	v_mov_b32_e32 v4, s6
	v_readlane_b32 s6, v254, 62
	v_ashrrev_i32_e32 v2, 8, v2
	v_add_u32_e32 v0, v2, v0
	v_mov_b32_e32 v5, s6
	ds_write_b32 v5, v0
	v_readlane_b32 s6, v254, 63
	s_waitcnt vmcnt(0)
	v_min_i32_e32 v2, 0x4000, v13
	ds_write_b32 v4, v2
	v_add_u32_e32 v2, 0xff, v2
	v_mov_b32_e32 v4, s6
	v_readlane_b32 s6, v255, 0
	v_ashrrev_i32_e32 v2, 8, v2
	v_add_u32_e32 v0, v2, v0
	v_mov_b32_e32 v5, s6
	ds_write_b32 v5, v0
	v_readlane_b32 s6, v255, 1
	s_waitcnt vmcnt(0)
	v_min_i32_e32 v2, 0x4000, v14
	ds_write_b32 v4, v2
	v_add_u32_e32 v2, 0xff, v2
	v_mov_b32_e32 v4, s6
	v_readlane_b32 s6, v255, 2
	v_ashrrev_i32_e32 v2, 8, v2
	v_add_u32_e32 v0, v2, v0
	v_mov_b32_e32 v5, s6
	ds_write_b32 v5, v0
	v_readlane_b32 s6, v255, 3
	s_waitcnt vmcnt(0)
	v_min_i32_e32 v2, 0x4000, v15
	ds_write_b32 v4, v2
	v_add_u32_e32 v2, 0xff, v2
	v_mov_b32_e32 v4, s6
	v_readlane_b32 s6, v255, 4
	v_ashrrev_i32_e32 v2, 8, v2
	v_add_u32_e32 v0, v2, v0
	v_mov_b32_e32 v5, s6
	ds_write_b32 v5, v0
	v_readlane_b32 s6, v255, 5
	s_waitcnt vmcnt(0)
	v_min_i32_e32 v2, 0x4000, v16
	ds_write_b32 v4, v2
	v_add_u32_e32 v2, 0xff, v2
	v_mov_b32_e32 v4, s6
	v_readlane_b32 s6, v255, 6
	v_ashrrev_i32_e32 v2, 8, v2
	v_add_u32_e32 v0, v2, v0
	v_mov_b32_e32 v5, s6
	ds_write_b32 v5, v0
	v_readlane_b32 s6, v255, 7
	s_waitcnt vmcnt(0)
	v_min_i32_e32 v2, 0x4000, v17
	ds_write_b32 v4, v2
	v_add_u32_e32 v2, 0xff, v2
	v_mov_b32_e32 v4, s6
	v_readlane_b32 s6, v255, 8
	v_ashrrev_i32_e32 v2, 8, v2
	v_add_u32_e32 v0, v2, v0
	v_mov_b32_e32 v5, s6
	ds_write_b32 v5, v0
	v_readlane_b32 s6, v255, 9
	s_waitcnt vmcnt(0)
	v_min_i32_e32 v2, 0x4000, v18
	ds_write_b32 v4, v2
	v_add_u32_e32 v2, 0xff, v2
	v_mov_b32_e32 v4, s6
	v_readlane_b32 s6, v255, 10
	v_ashrrev_i32_e32 v2, 8, v2
	v_add_u32_e32 v0, v2, v0
	v_mov_b32_e32 v5, s6
	ds_write_b32 v5, v0
	v_readlane_b32 s6, v255, 11
	s_waitcnt vmcnt(0)
	v_min_i32_e32 v2, 0x4000, v19
	ds_write_b32 v4, v2
	v_add_u32_e32 v2, 0xff, v2
	v_mov_b32_e32 v4, s6
	v_readlane_b32 s6, v255, 12
	v_ashrrev_i32_e32 v2, 8, v2
	v_add_u32_e32 v0, v2, v0
	v_mov_b32_e32 v5, s6
	ds_write_b32 v5, v0
	v_readlane_b32 s6, v255, 13
	s_waitcnt vmcnt(0)
	v_min_i32_e32 v2, 0x4000, v20
	ds_write_b32 v4, v2
	v_add_u32_e32 v2, 0xff, v2
	v_mov_b32_e32 v4, s6
	v_readlane_b32 s6, v255, 14
	v_ashrrev_i32_e32 v2, 8, v2
	v_add_u32_e32 v0, v2, v0
	v_mov_b32_e32 v5, s6
	ds_write_b32 v5, v0
	v_readlane_b32 s6, v255, 15
	s_waitcnt vmcnt(0)
	v_min_i32_e32 v2, 0x4000, v21
	ds_write_b32 v4, v2
	v_add_u32_e32 v2, 0xff, v2
	v_ashrrev_i32_e32 v2, 8, v2
	v_mov_b32_e32 v4, s6
	v_add_u32_e32 v0, v2, v0
	v_readlane_b32 s6, v255, 16
	s_waitcnt vmcnt(0)
	v_min_i32_e32 v2, 0x4000, v22
	ds_write_b32 v4, v2
	v_add_u32_e32 v2, 0xff, v2
	v_ashrrev_i32_e32 v2, 8, v2
	v_add_u32_e32 v2, v2, v0
	v_mov_b32_e32 v3, s6
	ds_write2_b32 v3, v0, v2 offset1:1

.LBB0_1434:
	s_andn2_b64 vcc, exec, s[4:5]
	s_cbranch_vccnz .LBB0_1529
	s_mov_b64 s[4:5], s[70:71]
	v_mbcnt_lo_u32_b32 v0, -1, 0
	v_mbcnt_hi_u32_b32 v0, -1, v0
	s_load_dwordx2 s[4:5], s[4:5], 0x100
	v_add_u32_e32 v2, s67, v0
	v_cmp_eq_u32_e32 vcc, 0, v2
	s_and_saveexec_b64 s[6:7], vcc
	s_cbranch_execz .LBB0_1437
	s_lshl_b32 s20, s88, 10
	s_lshl_b64 s[8:9], s[20:21], 2
	s_waitcnt lgkmcnt(0)
	s_add_u32 s8, s4, s8
	s_addc_u32 s9, s5, s9
	v_mov_b32_e32 v3, 0x10000
	global_load_dword v3, v3, s[8:9] sc1
	v_readlane_b32 s10, v254, 50
	v_mov_b32_e32 v5, s81
	s_add_u32 s8, s8, 0x10000
	v_mov_b32_e32 v4, s10
	ds_write_b32 v5, v1
	s_addc_u32 s9, s9, 0
	v_readlane_b32 s10, v254, 51
	s_waitcnt vmcnt(0)
	v_min_i32_e32 v3, 0x4000, v3
	ds_write_b32 v4, v3
	global_load_dword v8, v1, s[8:9] offset:256 sc1
	global_load_dword v9, v1, s[8:9] offset:512 sc1
	global_load_dword v10, v1, s[8:9] offset:768 sc1
	global_load_dword v11, v1, s[8:9] offset:1024 sc1
	global_load_dword v12, v1, s[8:9] offset:1280 sc1
	global_load_dword v13, v1, s[8:9] offset:1536 sc1
	global_load_dword v14, v1, s[8:9] offset:1792 sc1
	global_load_dword v15, v1, s[8:9] offset:2048 sc1
	global_load_dword v16, v1, s[8:9] offset:2304 sc1
	global_load_dword v17, v1, s[8:9] offset:2560 sc1
	global_load_dword v18, v1, s[8:9] offset:2816 sc1
	global_load_dword v19, v1, s[8:9] offset:3072 sc1
	global_load_dword v20, v1, s[8:9] offset:3328 sc1
	global_load_dword v21, v1, s[8:9] offset:3584 sc1
	global_load_dword v22, v1, s[8:9] offset:3840 sc1
	v_mov_b32_e32 v5, s10
	v_readlane_b32 s10, v254, 52
	v_add_u32_e32 v3, 0xff, v3
	v_ashrrev_i32_e32 v3, 8, v3
	v_mov_b32_e32 v6, s10
	ds_write_b32 v6, v3
	v_readlane_b32 s10, v254, 53
	s_waitcnt vmcnt(0)
	v_min_i32_e32 v4, 0x4000, v8
	ds_write_b32 v5, v4
	v_add_u32_e32 v4, 0xff, v4
	v_mov_b32_e32 v6, s10
	v_readlane_b32 s10, v254, 54
	v_ashrrev_i32_e32 v4, 8, v4
	v_add_u32_e32 v3, v4, v3
	v_mov_b32_e32 v7, s10
	ds_write_b32 v7, v3
	v_readlane_b32 s10, v254, 55
	s_waitcnt vmcnt(0)
	v_min_i32_e32 v4, 0x4000, v9
	ds_write_b32 v6, v4
	v_add_u32_e32 v4, 0xff, v4
	v_mov_b32_e32 v6, s10
	v_readlane_b32 s10, v254, 56
	v_ashrrev_i32_e32 v4, 8, v4
	v_add_u32_e32 v3, v4, v3
	v_mov_b32_e32 v7, s10
	ds_write_b32 v7, v3
	v_readlane_b32 s10, v254, 57
	s_waitcnt vmcnt(0)
	v_min_i32_e32 v4, 0x4000, v10
	ds_write_b32 v6, v4
	v_add_u32_e32 v4, 0xff, v4
	v_mov_b32_e32 v6, s10
	v_readlane_b32 s10, v254, 58
	v_ashrrev_i32_e32 v4, 8, v4
	v_add_u32_e32 v3, v4, v3
	v_mov_b32_e32 v7, s10
	ds_write_b32 v7, v3
	v_readlane_b32 s10, v254, 59
	s_waitcnt vmcnt(0)
	v_min_i32_e32 v4, 0x4000, v11
	ds_write_b32 v6, v4
	v_add_u32_e32 v4, 0xff, v4
	v_mov_b32_e32 v6, s10
	v_readlane_b32 s10, v254, 60
	v_ashrrev_i32_e32 v4, 8, v4
	v_add_u32_e32 v3, v4, v3
	v_mov_b32_e32 v7, s10
	ds_write_b32 v7, v3
	v_readlane_b32 s10, v254, 61
	s_waitcnt vmcnt(0)
	v_min_i32_e32 v4, 0x4000, v12
	ds_write_b32 v6, v4
	v_add_u32_e32 v4, 0xff, v4
	v_mov_b32_e32 v6, s10
	v_readlane_b32 s10, v254, 62
	v_ashrrev_i32_e32 v4, 8, v4
	v_add_u32_e32 v3, v4, v3
	v_mov_b32_e32 v7, s10
	ds_write_b32 v7, v3
	v_readlane_b32 s10, v254, 63
	s_waitcnt vmcnt(0)
	v_min_i32_e32 v4, 0x4000, v13
	ds_write_b32 v6, v4
	v_add_u32_e32 v4, 0xff, v4
	v_mov_b32_e32 v6, s10
	v_readlane_b32 s10, v255, 0
	v_ashrrev_i32_e32 v4, 8, v4
	v_add_u32_e32 v3, v4, v3
	v_mov_b32_e32 v7, s10
	ds_write_b32 v7, v3
	v_readlane_b32 s10, v255, 1
	s_waitcnt vmcnt(0)
	v_min_i32_e32 v4, 0x4000, v14
	ds_write_b32 v6, v4
	v_add_u32_e32 v4, 0xff, v4
	v_mov_b32_e32 v6, s10
	v_readlane_b32 s10, v255, 2
	v_ashrrev_i32_e32 v4, 8, v4
	v_add_u32_e32 v3, v4, v3
	v_mov_b32_e32 v7, s10
	ds_write_b32 v7, v3
	v_readlane_b32 s10, v255, 3
	s_waitcnt vmcnt(0)
	v_min_i32_e32 v4, 0x4000, v15
	ds_write_b32 v6, v4
	v_add_u32_e32 v4, 0xff, v4
	v_mov_b32_e32 v6, s10
	v_readlane_b32 s10, v255, 4
	v_ashrrev_i32_e32 v4, 8, v4
	v_add_u32_e32 v3, v4, v3
	v_mov_b32_e32 v7, s10
	ds_write_b32 v7, v3
	v_readlane_b32 s10, v255, 5
	s_waitcnt vmcnt(0)
	v_min_i32_e32 v4, 0x4000, v16
	ds_write_b32 v6, v4
	v_add_u32_e32 v4, 0xff, v4
	v_mov_b32_e32 v6, s10
	v_readlane_b32 s10, v255, 6
	v_ashrrev_i32_e32 v4, 8, v4
	v_add_u32_e32 v3, v4, v3
	v_mov_b32_e32 v7, s10
	ds_write_b32 v7, v3
	v_readlane_b32 s10, v255, 7
	s_waitcnt vmcnt(0)
	v_min_i32_e32 v4, 0x4000, v17
	ds_write_b32 v6, v4
	v_add_u32_e32 v4, 0xff, v4
	v_mov_b32_e32 v6, s10
	v_readlane_b32 s10, v255, 8
	v_ashrrev_i32_e32 v4, 8, v4
	v_add_u32_e32 v3, v4, v3
	v_mov_b32_e32 v7, s10
	ds_write_b32 v7, v3
	v_readlane_b32 s10, v255, 9
	s_waitcnt vmcnt(0)
	v_min_i32_e32 v4, 0x4000, v18
	ds_write_b32 v6, v4
	v_add_u32_e32 v4, 0xff, v4
	v_mov_b32_e32 v6, s10
	v_readlane_b32 s10, v255, 10
	v_ashrrev_i32_e32 v4, 8, v4
	v_add_u32_e32 v3, v4, v3
	v_mov_b32_e32 v7, s10
	ds_write_b32 v7, v3
	v_readlane_b32 s10, v255, 11
	s_waitcnt vmcnt(0)
	v_min_i32_e32 v4, 0x4000, v19
	ds_write_b32 v6, v4
	v_add_u32_e32 v4, 0xff, v4
	v_mov_b32_e32 v6, s10
	v_readlane_b32 s10, v255, 12
	v_ashrrev_i32_e32 v4, 8, v4
	v_add_u32_e32 v3, v4, v3
	v_mov_b32_e32 v7, s10
	ds_write_b32 v7, v3
	v_readlane_b32 s10, v255, 13
	s_waitcnt vmcnt(0)
	v_min_i32_e32 v4, 0x4000, v20
	ds_write_b32 v6, v4
	v_add_u32_e32 v4, 0xff, v4
	v_mov_b32_e32 v6, s10
	v_readlane_b32 s10, v255, 14
	v_ashrrev_i32_e32 v4, 8, v4
	v_add_u32_e32 v3, v4, v3
	v_mov_b32_e32 v7, s10
	ds_write_b32 v7, v3
	s_waitcnt vmcnt(0)
	v_min_i32_e32 v4, 0x4000, v21
	ds_write_b32 v6, v4
	v_add_u32_e32 v4, 0xff, v4
	v_readlane_b32 s8, v255, 15
	v_ashrrev_i32_e32 v4, 8, v4
	v_add_u32_e32 v3, v4, v3
	v_mov_b32_e32 v6, s8
	v_readlane_b32 s8, v255, 16
	s_waitcnt vmcnt(0)
	v_min_i32_e32 v4, 0x4000, v22
	ds_write_b32 v6, v4
	v_add_u32_e32 v4, 0xff, v4
	v_ashrrev_i32_e32 v4, 8, v4
	v_add_u32_e32 v4, v4, v3
	v_mov_b32_e32 v5, s8
	ds_write2_b32 v5, v3, v4 offset1:1

.LBB0_1530:
	s_mov_b64 s[4:5], s[70:71]
	v_mbcnt_lo_u32_b32 v14, -1, 0
	v_mbcnt_hi_u32_b32 v14, -1, v14
	s_load_dwordx2 s[8:9], s[4:5], 0x100
	v_add_u32_e32 v0, s67, v14
	v_cmp_eq_u32_e32 vcc, 0, v0
	s_and_saveexec_b64 s[4:5], vcc
	s_cbranch_execz .LBB0_1532
	s_lshl_b32 s20, s88, 10
	s_lshl_b64 s[6:7], s[20:21], 2
	s_waitcnt lgkmcnt(0)
	s_add_u32 s6, s8, s6
	s_addc_u32 s7, s9, s7
	v_mov_b32_e32 v2, 0x10000
	global_load_dword v2, v2, s[6:7] sc1
	v_readlane_b32 s10, v254, 50
	v_mov_b32_e32 v4, s81
	s_add_u32 s6, s6, 0x10000
	v_mov_b32_e32 v3, s10
	ds_write_b32 v4, v1
	s_addc_u32 s7, s7, 0
	v_readlane_b32 s10, v254, 51
	s_waitcnt vmcnt(0)
	v_min_i32_e32 v2, 0x4000, v2
	ds_write_b32 v3, v2
	global_load_dword v8, v1, s[6:7] offset:256 sc1
	global_load_dword v9, v1, s[6:7] offset:512 sc1
	global_load_dword v10, v1, s[6:7] offset:768 sc1
	global_load_dword v11, v1, s[6:7] offset:1024 sc1
	global_load_dword v12, v1, s[6:7] offset:1280 sc1
	global_load_dword v13, v1, s[6:7] offset:1536 sc1
	global_load_dword v15, v1, s[6:7] offset:1792 sc1
	global_load_dword v16, v1, s[6:7] offset:2048 sc1
	global_load_dword v17, v1, s[6:7] offset:2304 sc1
	global_load_dword v18, v1, s[6:7] offset:2560 sc1
	global_load_dword v19, v1, s[6:7] offset:2816 sc1
	global_load_dword v20, v1, s[6:7] offset:3072 sc1
	global_load_dword v21, v1, s[6:7] offset:3328 sc1
	global_load_dword v22, v1, s[6:7] offset:3584 sc1
	global_load_dword v23, v1, s[6:7] offset:3840 sc1
	v_mov_b32_e32 v4, s10
	v_readlane_b32 s10, v254, 52
	v_add_u32_e32 v2, 0xff, v2
	v_ashrrev_i32_e32 v2, 8, v2
	v_mov_b32_e32 v5, s10
	ds_write_b32 v5, v2
	v_readlane_b32 s10, v254, 53
	s_waitcnt vmcnt(0)
	v_min_i32_e32 v3, 0x4000, v8
	ds_write_b32 v4, v3
	v_add_u32_e32 v3, 0xff, v3
	v_mov_b32_e32 v5, s10
	v_readlane_b32 s10, v254, 54
	v_ashrrev_i32_e32 v3, 8, v3
	v_add_u32_e32 v2, v3, v2
	v_mov_b32_e32 v6, s10
	ds_write_b32 v6, v2
	v_readlane_b32 s10, v254, 55
	s_waitcnt vmcnt(0)
	v_min_i32_e32 v3, 0x4000, v9
	ds_write_b32 v5, v3
	v_add_u32_e32 v3, 0xff, v3
	v_mov_b32_e32 v5, s10
	v_readlane_b32 s10, v254, 56
	v_ashrrev_i32_e32 v3, 8, v3
	v_add_u32_e32 v2, v3, v2
	v_mov_b32_e32 v6, s10
	ds_write_b32 v6, v2
	v_readlane_b32 s10, v254, 57
	s_waitcnt vmcnt(0)
	v_min_i32_e32 v3, 0x4000, v10
	ds_write_b32 v5, v3
	v_add_u32_e32 v3, 0xff, v3
	v_mov_b32_e32 v5, s10
	v_readlane_b32 s10, v254, 58
	v_ashrrev_i32_e32 v3, 8, v3
	v_add_u32_e32 v2, v3, v2
	v_mov_b32_e32 v6, s10
	ds_write_b32 v6, v2
	v_readlane_b32 s10, v254, 59
	s_waitcnt vmcnt(0)
	v_min_i32_e32 v3, 0x4000, v11
	ds_write_b32 v5, v3
	v_add_u32_e32 v3, 0xff, v3
	v_mov_b32_e32 v5, s10
	v_readlane_b32 s10, v254, 60
	v_ashrrev_i32_e32 v3, 8, v3
	v_add_u32_e32 v2, v3, v2
	v_mov_b32_e32 v6, s10
	ds_write_b32 v6, v2
	v_readlane_b32 s10, v254, 61
	s_waitcnt vmcnt(0)
	v_min_i32_e32 v3, 0x4000, v12
	ds_write_b32 v5, v3
	v_add_u32_e32 v3, 0xff, v3
	v_mov_b32_e32 v5, s10
	v_readlane_b32 s10, v254, 62
	v_ashrrev_i32_e32 v3, 8, v3
	v_add_u32_e32 v2, v3, v2
	v_mov_b32_e32 v6, s10
	ds_write_b32 v6, v2
	v_readlane_b32 s10, v254, 63
	s_waitcnt vmcnt(0)
	v_min_i32_e32 v3, 0x4000, v13
	ds_write_b32 v5, v3
	v_add_u32_e32 v3, 0xff, v3
	v_mov_b32_e32 v5, s10
	v_readlane_b32 s10, v255, 0
	v_ashrrev_i32_e32 v3, 8, v3
	v_add_u32_e32 v2, v3, v2
	v_mov_b32_e32 v6, s10
	ds_write_b32 v6, v2
	v_readlane_b32 s10, v255, 1
	s_waitcnt vmcnt(0)
	v_min_i32_e32 v3, 0x4000, v15
	ds_write_b32 v5, v3
	v_add_u32_e32 v3, 0xff, v3
	v_mov_b32_e32 v5, s10
	v_readlane_b32 s10, v255, 2
	v_ashrrev_i32_e32 v3, 8, v3
	v_add_u32_e32 v2, v3, v2
	v_mov_b32_e32 v6, s10
	ds_write_b32 v6, v2
	v_readlane_b32 s10, v255, 3
	s_waitcnt vmcnt(0)
	v_min_i32_e32 v3, 0x4000, v16
	ds_write_b32 v5, v3
	v_add_u32_e32 v3, 0xff, v3
	v_mov_b32_e32 v5, s10
	v_readlane_b32 s10, v255, 4
	v_ashrrev_i32_e32 v3, 8, v3
	v_add_u32_e32 v2, v3, v2
	v_mov_b32_e32 v6, s10
	ds_write_b32 v6, v2
	v_readlane_b32 s10, v255, 5
	s_waitcnt vmcnt(0)
	v_min_i32_e32 v3, 0x4000, v17
	ds_write_b32 v5, v3
	v_add_u32_e32 v3, 0xff, v3
	v_mov_b32_e32 v5, s10
	v_readlane_b32 s10, v255, 6
	v_ashrrev_i32_e32 v3, 8, v3
	v_add_u32_e32 v2, v3, v2
	v_mov_b32_e32 v6, s10
	ds_write_b32 v6, v2
	v_readlane_b32 s10, v255, 7
	s_waitcnt vmcnt(0)
	v_min_i32_e32 v3, 0x4000, v18
	ds_write_b32 v5, v3
	v_add_u32_e32 v3, 0xff, v3
	v_mov_b32_e32 v5, s10
	v_readlane_b32 s10, v255, 8
	v_ashrrev_i32_e32 v3, 8, v3
	v_add_u32_e32 v2, v3, v2
	v_mov_b32_e32 v6, s10
	ds_write_b32 v6, v2
	v_readlane_b32 s10, v255, 9
	s_waitcnt vmcnt(0)
	v_min_i32_e32 v3, 0x4000, v19
	ds_write_b32 v5, v3
	v_add_u32_e32 v3, 0xff, v3
	v_mov_b32_e32 v5, s10
	v_readlane_b32 s10, v255, 10
	v_ashrrev_i32_e32 v3, 8, v3
	v_add_u32_e32 v2, v3, v2
	v_mov_b32_e32 v6, s10
	ds_write_b32 v6, v2
	v_readlane_b32 s10, v255, 11
	s_waitcnt vmcnt(0)
	v_min_i32_e32 v3, 0x4000, v20
	ds_write_b32 v5, v3
	v_add_u32_e32 v3, 0xff, v3
	v_mov_b32_e32 v5, s10
	v_readlane_b32 s10, v255, 12
	v_ashrrev_i32_e32 v3, 8, v3
	v_add_u32_e32 v2, v3, v2
	v_mov_b32_e32 v6, s10
	ds_write_b32 v6, v2
	v_readlane_b32 s10, v255, 13
	s_waitcnt vmcnt(0)
	v_min_i32_e32 v3, 0x4000, v21
	ds_write_b32 v5, v3
	v_add_u32_e32 v3, 0xff, v3
	v_mov_b32_e32 v5, s10
	v_readlane_b32 s10, v255, 14
	v_ashrrev_i32_e32 v3, 8, v3
	v_add_u32_e32 v2, v3, v2
	v_mov_b32_e32 v6, s10
	ds_write_b32 v6, v2
	s_waitcnt vmcnt(0)
	v_min_i32_e32 v3, 0x4000, v22
	ds_write_b32 v5, v3
	v_add_u32_e32 v3, 0xff, v3
	v_readlane_b32 s6, v255, 15
	v_ashrrev_i32_e32 v3, 8, v3
	v_add_u32_e32 v2, v3, v2
	v_mov_b32_e32 v5, s6
	v_readlane_b32 s6, v255, 16
	s_waitcnt vmcnt(0)
	v_min_i32_e32 v3, 0x4000, v23
	ds_write_b32 v5, v3
	v_add_u32_e32 v3, 0xff, v3
	v_ashrrev_i32_e32 v3, 8, v3
	v_add_u32_e32 v3, v3, v2
	v_mov_b32_e32 v4, s6
	ds_write2_b32 v4, v2, v3 offset1:1

.LBB0_1606:
	s_cmp_lt_i32 s86, 24
	s_cselect_b64 s[0:1], -1, 0
	s_cmp_gt_i32 s87, 23
	s_cselect_b64 s[2:3], -1, 0
	s_and_b64 s[0:1], s[0:1], s[2:3]
	s_and_b64 vcc, exec, s[0:1]
	s_cbranch_vccz .LBB0_1614
	v_mbcnt_lo_u32_b32 v0, -1, 0
	v_mbcnt_hi_u32_b32 v0, -1, v0
	s_load_dwordx2 s[0:1], s[70:71], 0x100
	v_add_u32_e32 v1, s67, v0
	s_mov_b32 s5, 0
	v_readfirstlane_b32 s4, v1
	v_cmp_eq_u32_e32 vcc, 0, v1
	s_and_saveexec_b64 s[2:3], vcc
	s_cbranch_execz .LBB0_1609
	v_mov_b32_e32 v1, 0x11000
	s_waitcnt lgkmcnt(0)
	global_load_dword v2, v1, s[0:1] sc1
	s_add_i32 s6, 0, 0x200c0
	s_add_i32 s7, 0, 0x20040
	v_mov_b32_e32 v3, 0
	v_mov_b32_e32 v4, s6
	v_mov_b32_e32 v5, s7
	ds_write_b32 v5, v3
	s_add_i32 s6, 0, 0x200c4
	s_add_i32 s7, 0, 0x20044
	v_mov_b32_e32 v5, s7
	s_add_i32 s7, 0, 0x20048
	v_mov_b32_e32 v6, s7
	s_add_i32 s7, 0, 0x2004c
	s_waitcnt vmcnt(0)
	v_min_i32_e32 v2, 0x4000, v2
	ds_write_b32 v4, v2
	global_load_dword v8, v1, s[0:1] offset:256 sc1
	global_load_dword v9, v1, s[0:1] offset:512 sc1
	global_load_dword v10, v1, s[0:1] offset:768 sc1
	global_load_dword v11, v1, s[0:1] offset:1024 sc1
	global_load_dword v12, v1, s[0:1] offset:1280 sc1
	global_load_dword v13, v1, s[0:1] offset:1536 sc1
	global_load_dword v14, v1, s[0:1] offset:1792 sc1
	global_load_dword v15, v1, s[0:1] offset:2048 sc1
	global_load_dword v16, v1, s[0:1] offset:2304 sc1
	global_load_dword v17, v1, s[0:1] offset:2560 sc1
	global_load_dword v18, v1, s[0:1] offset:2816 sc1
	global_load_dword v19, v1, s[0:1] offset:3072 sc1
	global_load_dword v20, v1, s[0:1] offset:3328 sc1
	global_load_dword v21, v1, s[0:1] offset:3584 sc1
	global_load_dword v22, v1, s[0:1] offset:3840 sc1
	v_add_u32_e32 v2, 0xff, v2
	v_mov_b32_e32 v4, s6
	v_ashrrev_i32_e32 v2, 8, v2
	ds_write_b32 v5, v2
	s_add_i32 s6, 0, 0x200c8
	v_mov_b32_e32 v5, s6
	s_add_i32 s6, 0, 0x200cc
	s_waitcnt vmcnt(0)
	v_min_i32_e32 v3, 0x4000, v8
	ds_write_b32 v4, v3
	v_add_u32_e32 v3, 0xff, v3
	v_ashrrev_i32_e32 v3, 8, v3
	v_add_u32_e32 v2, v3, v2
	ds_write_b32 v6, v2
	v_mov_b32_e32 v6, s7
	s_add_i32 s7, 0, 0x20050
	s_waitcnt vmcnt(0)
	v_min_i32_e32 v3, 0x4000, v9
	ds_write_b32 v5, v3
	v_add_u32_e32 v3, 0xff, v3
	v_ashrrev_i32_e32 v3, 8, v3
	v_mov_b32_e32 v5, s6
	v_add_u32_e32 v2, v3, v2
	ds_write_b32 v6, v2
	s_add_i32 s6, 0, 0x200d0
	v_mov_b32_e32 v6, s7
	s_add_i32 s7, 0, 0x20054
	s_waitcnt vmcnt(0)
	v_min_i32_e32 v3, 0x4000, v10
	ds_write_b32 v5, v3
	v_add_u32_e32 v3, 0xff, v3
	v_ashrrev_i32_e32 v3, 8, v3
	v_mov_b32_e32 v5, s6
	v_add_u32_e32 v2, v3, v2
	ds_write_b32 v6, v2
	s_add_i32 s6, 0, 0x200d4
	v_mov_b32_e32 v6, s7
	s_add_i32 s7, 0, 0x20058
	s_waitcnt vmcnt(0)
	v_min_i32_e32 v3, 0x4000, v11
	ds_write_b32 v5, v3
	v_add_u32_e32 v3, 0xff, v3
	v_ashrrev_i32_e32 v3, 8, v3
	v_mov_b32_e32 v5, s6
	v_add_u32_e32 v2, v3, v2
	ds_write_b32 v6, v2
	s_add_i32 s6, 0, 0x200d8
	v_mov_b32_e32 v6, s7
	s_add_i32 s7, 0, 0x2005c
	s_waitcnt vmcnt(0)
	v_min_i32_e32 v3, 0x4000, v12
	ds_write_b32 v5, v3
	v_add_u32_e32 v3, 0xff, v3
	v_ashrrev_i32_e32 v3, 8, v3
	v_mov_b32_e32 v5, s6
	v_add_u32_e32 v2, v3, v2
	ds_write_b32 v6, v2
	s_add_i32 s6, 0, 0x200dc
	v_mov_b32_e32 v6, s7
	s_add_i32 s7, 0, 0x20060
	s_waitcnt vmcnt(0)
	v_min_i32_e32 v3, 0x4000, v13
	ds_write_b32 v5, v3
	v_add_u32_e32 v3, 0xff, v3
	v_ashrrev_i32_e32 v3, 8, v3
	v_mov_b32_e32 v5, s6
	v_add_u32_e32 v2, v3, v2
	ds_write_b32 v6, v2
	s_add_i32 s6, 0, 0x200e0
	v_mov_b32_e32 v6, s7
	s_add_i32 s7, 0, 0x20064
	s_waitcnt vmcnt(0)
	v_min_i32_e32 v3, 0x4000, v14
	ds_write_b32 v5, v3
	v_add_u32_e32 v3, 0xff, v3
	v_ashrrev_i32_e32 v3, 8, v3
	v_mov_b32_e32 v5, s6
	v_add_u32_e32 v2, v3, v2
	ds_write_b32 v6, v2
	s_add_i32 s6, 0, 0x200e4
	v_mov_b32_e32 v6, s7
	s_add_i32 s7, 0, 0x20068
	s_waitcnt vmcnt(0)
	v_min_i32_e32 v3, 0x4000, v15
	ds_write_b32 v5, v3
	v_add_u32_e32 v3, 0xff, v3
	v_ashrrev_i32_e32 v3, 8, v3
	v_mov_b32_e32 v5, s6
	v_add_u32_e32 v2, v3, v2
	ds_write_b32 v6, v2
	s_add_i32 s6, 0, 0x200e8
	v_mov_b32_e32 v6, s7
	s_add_i32 s7, 0, 0x2006c
	s_waitcnt vmcnt(0)
	v_min_i32_e32 v3, 0x4000, v16
	ds_write_b32 v5, v3
	v_add_u32_e32 v3, 0xff, v3
	v_ashrrev_i32_e32 v3, 8, v3
	v_mov_b32_e32 v5, s6
	v_add_u32_e32 v2, v3, v2
	ds_write_b32 v6, v2
	s_add_i32 s6, 0, 0x200ec
	v_mov_b32_e32 v6, s7
	s_add_i32 s7, 0, 0x20070
	s_waitcnt vmcnt(0)
	v_min_i32_e32 v3, 0x4000, v17
	ds_write_b32 v5, v3
	v_add_u32_e32 v3, 0xff, v3
	v_ashrrev_i32_e32 v3, 8, v3
	v_mov_b32_e32 v5, s6
	v_add_u32_e32 v2, v3, v2
	ds_write_b32 v6, v2
	s_add_i32 s6, 0, 0x200f0
	v_mov_b32_e32 v6, s7
	s_add_i32 s7, 0, 0x20074
	s_waitcnt vmcnt(0)
	v_min_i32_e32 v3, 0x4000, v18
	ds_write_b32 v5, v3
	v_add_u32_e32 v3, 0xff, v3
	v_ashrrev_i32_e32 v3, 8, v3
	v_mov_b32_e32 v5, s6
	v_add_u32_e32 v2, v3, v2
	ds_write_b32 v6, v2
	s_add_i32 s6, 0, 0x200f4
	v_mov_b32_e32 v6, s7
	s_add_i32 s7, 0, 0x20078
	s_waitcnt vmcnt(0)
	v_min_i32_e32 v3, 0x4000, v19
	ds_write_b32 v5, v3
	v_add_u32_e32 v3, 0xff, v3
	v_ashrrev_i32_e32 v3, 8, v3
	v_mov_b32_e32 v5, s6
	v_add_u32_e32 v2, v3, v2
	ds_write_b32 v6, v2
	s_add_i32 s6, 0, 0x200f8
	v_mov_b32_e32 v6, s7
	s_add_i32 s7, 0, 0x2007c
	s_waitcnt vmcnt(0)
	v_min_i32_e32 v3, 0x4000, v20
	ds_write_b32 v5, v3
	v_add_u32_e32 v3, 0xff, v3
	v_ashrrev_i32_e32 v3, 8, v3
	v_mov_b32_e32 v5, s6
	v_add_u32_e32 v2, v3, v2
	ds_write_b32 v6, v2
	s_add_i32 s6, 0, 0x200fc
	s_waitcnt vmcnt(0)
	v_min_i32_e32 v3, 0x4000, v21
	ds_write_b32 v5, v3
	v_mov_b32_e32 v4, s6
	v_add_u32_e32 v3, 0xff, v3
	v_ashrrev_i32_e32 v3, 8, v3
	v_add_u32_e32 v2, v3, v2
	v_mov_b32_e32 v3, s7
	s_waitcnt vmcnt(0)
	v_min_i32_e32 v1, 0x4000, v22
	ds_write_b32 v4, v1
	v_add_u32_e32 v1, 0xff, v1
	v_ashrrev_i32_e32 v1, 8, v1
	v_add_u32_e32 v1, v1, v2
	ds_write2_b32 v3, v2, v1 offset1:1
